# grid barrier: each XCD leader adds to all per-XCD arrival words after its L2 write-back; every block polls its own XCD word for the arrival count (no top-level round trip, no relay)
# speedup vs baseline: 1.0131x; 1.0131x over previous
.LBB0_158:
	s_or_b64 exec, exec, s[2:3]
	v_mov_b32_e32 v1, s25
	v_add_co_u32_e32 v4, vcc, 0x2000, v1
	v_mov_b32_e32 v1, s24
	s_nop 0
	v_addc_co_u32_e32 v5, vcc, 0, v1, vcc
	s_waitcnt vmcnt(0) lgkmcnt(0)
	buffer_inv sc1
	s_waitcnt vmcnt(0)

.LBB0_193:
	v_readlane_b32 s4, v251, 48
	s_lshl_b32 s4, s4, 2
	s_add_u32 s25, s2, s4
	s_addc_u32 s24, s3, 0
	v_mov_b32_e32 v1, s25
	v_add_co_u32_e32 v8, vcc, 0x1000, v1
	v_mov_b32_e32 v1, s24
	s_nop 0
	v_addc_co_u32_e32 v9, vcc, 0, v1, vcc
	flat_atomic_add v1, v[8:9], v211 offset:1024 sc0
	v_cvt_f32_u32_e32 v3, v6
	v_sub_u32_e32 v5, 0, v6
	v_rcp_iflag_f32_e32 v3, v3
	s_nop 0
	v_mul_f32_e32 v3, 0x4f7ffffe, v3
	v_cvt_u32_f32_e32 v3, v3
	v_mul_lo_u32 v5, v5, v3
	v_mul_hi_u32 v5, v3, v5
	v_add_u32_e32 v3, v3, v5
	s_waitcnt vmcnt(0) lgkmcnt(0)
	v_mul_hi_u32 v3, v1, v3
	v_mul_lo_u32 v7, v3, v6
	v_add_u32_e32 v5, 1, v1
	v_sub_u32_e32 v1, v1, v7
	v_add_u32_e32 v8, 1, v3
	v_cmp_ge_u32_e32 vcc, v1, v6
	v_sub_u32_e32 v7, v1, v6
	s_nop 0
	v_cndmask_b32_e32 v3, v3, v8, vcc
	v_cndmask_b32_e32 v1, v1, v7, vcc
	v_add_u32_e32 v7, 1, v3
	v_cmp_ge_u32_e32 vcc, v1, v6
	s_nop 1
	v_cndmask_b32_e32 v1, v3, v7, vcc
	v_mad_u64_u32 v[6:7], s[4:5], v6, v1, v[6:7]
	v_cmp_ne_u32_e32 vcc, v5, v6
	s_and_saveexec_b64 s[4:5], vcc
	s_xor_b64 s[4:5], exec, s[4:5]
	s_cbranch_execz .LBB0_206
	v_mad_u32_u24 v255, v4, v1, 1
	v_mov_b32_e32 v3, s25
	v_add_co_u32_e32 v4, vcc, 0x2000, v3
	v_mov_b32_e32 v3, s24
	s_nop 0
	v_addc_co_u32_e32 v5, vcc, 0, v3, vcc
	flat_load_dword v3, v[4:5] offset:1024 sc1
	s_add_u32 s8, s25, 0x2400
	s_addc_u32 s9, s24, 0
	s_waitcnt vmcnt(0) lgkmcnt(0)
	v_cmp_lt_u32_e32 vcc, v3, v255
	s_and_saveexec_b64 s[6:7], vcc
	s_cbranch_execz .LBB0_205
	s_mov_b32 s26, 1
	s_mov_b64 s[10:11], 0
	s_branch .LBB0_197

.LBB0_201:
	s_andn2_b64 s[14:15], s[14:15], exec
	s_and_b64 s[20:21], s[20:21], exec
	s_or_b64 s[14:15], s[14:15], s[20:21]
	s_and_saveexec_b64 s[20:21], s[18:19]
	s_cbranch_execz .LBB0_196
	v_mov_b64_e32 v[4:5], s[8:9]
	flat_load_dword v3, v[4:5] sc1
	s_add_i32 s26, s26, 1
	s_or_b64 s[14:15], s[14:15], exec
	s_waitcnt vmcnt(0) lgkmcnt(0)
	v_cmp_ge_u32_e32 vcc, v3, v255
	s_orn2_b64 s[16:17], vcc, exec
	s_branch .LBB0_196

.LBB0_206:
	s_andn2_saveexec_b64 s[4:5], s[4:5]
	s_cbranch_execz .LBB0_222
	v_mad_u32_u24 v255, v4, v1, 1
	buffer_wbl2 sc1
	s_waitcnt vmcnt(0)
	s_add_u32 s4, s2, 0x2400
	s_addc_u32 s5, s3, 0
	v_mov_b64_e32 v[4:5], s[4:5]
	flat_atomic_add v[4:5], v211
	flat_atomic_add v[4:5], v211 offset:256
	flat_atomic_add v[4:5], v211 offset:512
	flat_atomic_add v[4:5], v211 offset:768
	flat_atomic_add v[4:5], v211 offset:1024
	flat_atomic_add v[4:5], v211 offset:1280
	flat_atomic_add v[4:5], v211 offset:1536
	flat_atomic_add v[4:5], v211 offset:1792
	flat_atomic_add v[4:5], v211 offset:2048
	flat_atomic_add v[4:5], v211 offset:2304
	flat_atomic_add v[4:5], v211 offset:2560
	flat_atomic_add v[4:5], v211 offset:2816
	flat_atomic_add v[4:5], v211 offset:3072
	flat_atomic_add v[4:5], v211 offset:3328
	flat_atomic_add v[4:5], v211 offset:3584
	flat_atomic_add v[4:5], v211 offset:3840
	s_add_u32 s4, s25, 0x2400
	s_addc_u32 s5, s24, 0
	s_mov_b64 s[8:9], 0
	v_cmp_eq_u32_e32 vcc, v255, v255
	v_mov_b64_e32 v[4:5], s[4:5]
	s_and_saveexec_b64 s[6:7], vcc
	s_cbranch_execz .LBB0_219
	v_mov_b64_e32 v[4:5], s[4:5]
	flat_load_dword v3, v[4:5] sc1
	s_mov_b64 s[12:13], 0
	s_waitcnt vmcnt(0) lgkmcnt(0)
	v_cmp_lt_u32_e32 vcc, v3, v255
	s_and_saveexec_b64 s[10:11], vcc
	s_cbranch_execz .LBB0_218
	s_add_u32 s8, s2, 0x200
	s_addc_u32 s9, s3, 0
	s_mov_b32 s22, 1
	s_mov_b64 s[2:3], 0
	s_branch .LBB0_211

.LBB0_216:
	v_mov_b64_e32 v[4:5], s[4:5]
	flat_load_dword v3, v[4:5] sc1
	s_add_i32 s22, s22, 1
	s_or_b64 s[16:17], s[16:17], exec
	s_waitcnt vmcnt(0) lgkmcnt(0)
	v_cmp_ge_u32_e32 vcc, v3, v255
	s_orn2_b64 s[14:15], vcc, exec
	s_branch .LBB0_210

.LBB0_360:
	v_readlane_b32 s4, v251, 48
	s_lshl_b32 s4, s4, 2
	s_add_u32 s25, s2, s4
	s_addc_u32 s24, s3, 0
	v_mov_b32_e32 v1, s25
	v_add_co_u32_e32 v8, vcc, 0x1000, v1
	v_mov_b32_e32 v1, s24
	s_nop 0
	v_addc_co_u32_e32 v9, vcc, 0, v1, vcc
	flat_atomic_add v3, v[8:9], v211 offset:1024 sc0
	v_cvt_f32_u32_e32 v1, v6
	v_sub_u32_e32 v5, 0, v6
	v_rcp_iflag_f32_e32 v1, v1
	s_nop 0
	v_mul_f32_e32 v1, 0x4f7ffffe, v1
	v_cvt_u32_f32_e32 v1, v1
	v_mul_lo_u32 v5, v5, v1
	v_mul_hi_u32 v5, v1, v5
	v_add_u32_e32 v1, v1, v5
	s_waitcnt vmcnt(0) lgkmcnt(0)
	v_mul_hi_u32 v1, v3, v1
	v_mul_lo_u32 v5, v1, v6
	v_sub_u32_e32 v5, v3, v5
	v_cmp_ge_u32_e32 vcc, v5, v6
	v_add_u32_e32 v7, 1, v1
	v_add_u32_e32 v3, 1, v3
	v_cndmask_b32_e32 v1, v1, v7, vcc
	v_sub_u32_e32 v7, v5, v6
	v_cndmask_b32_e32 v5, v5, v7, vcc
	v_cmp_ge_u32_e32 vcc, v5, v6
	v_add_u32_e32 v5, 1, v1
	s_nop 0
	v_cndmask_b32_e32 v1, v1, v5, vcc
	v_mad_u64_u32 v[6:7], s[4:5], v6, v1, v[6:7]
	v_cmp_ne_u32_e32 vcc, v3, v6
	s_and_saveexec_b64 s[4:5], vcc
	s_xor_b64 s[4:5], exec, s[4:5]
	s_cbranch_execz .LBB0_373
	v_mad_u32_u24 v255, v4, v1, 1
	v_mov_b32_e32 v3, s25
	v_add_co_u32_e32 v4, vcc, 0x2000, v3
	v_mov_b32_e32 v3, s24
	s_nop 0
	v_addc_co_u32_e32 v5, vcc, 0, v3, vcc
	flat_load_dword v3, v[4:5] offset:1024 sc1
	s_add_u32 s8, s25, 0x2400
	s_addc_u32 s9, s24, 0
	s_waitcnt vmcnt(0) lgkmcnt(0)
	v_cmp_lt_u32_e32 vcc, v3, v255
	s_and_saveexec_b64 s[6:7], vcc
	s_cbranch_execz .LBB0_372
	s_mov_b32 s26, 1
	s_mov_b64 s[10:11], 0
	s_branch .LBB0_364

.LBB0_1326:
	v_mad_u32_u24 v255, v4, v1, 1
	buffer_wbl2 sc1
	s_waitcnt vmcnt(0)
	s_add_u32 s4, s2, 0x2400
	s_addc_u32 s5, s3, 0
	v_mov_b64_e32 v[4:5], s[4:5]
	flat_atomic_add v[4:5], v211
	flat_atomic_add v[4:5], v211 offset:256
	flat_atomic_add v[4:5], v211 offset:512
	flat_atomic_add v[4:5], v211 offset:768
	flat_atomic_add v[4:5], v211 offset:1024
	flat_atomic_add v[4:5], v211 offset:1280
	flat_atomic_add v[4:5], v211 offset:1536
	flat_atomic_add v[4:5], v211 offset:1792
	flat_atomic_add v[4:5], v211 offset:2048
	flat_atomic_add v[4:5], v211 offset:2304
	flat_atomic_add v[4:5], v211 offset:2560
	flat_atomic_add v[4:5], v211 offset:2816
	flat_atomic_add v[4:5], v211 offset:3072
	flat_atomic_add v[4:5], v211 offset:3328
	flat_atomic_add v[4:5], v211 offset:3584
	flat_atomic_add v[4:5], v211 offset:3840
	s_add_u32 s4, s25, 0x2400
	s_addc_u32 s5, s24, 0
	s_mov_b64 s[8:9], 0
	v_cmp_eq_u32_e32 vcc, v255, v255
	v_mov_b64_e32 v[4:5], s[4:5]
	s_and_saveexec_b64 s[6:7], vcc
	s_cbranch_execz .LBB0_1338
	v_mov_b64_e32 v[4:5], s[4:5]
	flat_load_dword v3, v[4:5] sc1
	s_mov_b64 s[12:13], 0
	s_waitcnt vmcnt(0) lgkmcnt(0)
	v_cmp_lt_u32_e32 vcc, v3, v255
	s_and_saveexec_b64 s[10:11], vcc
	s_cbranch_execz .LBB0_1337
	s_add_u32 s8, s2, 0x200
	s_addc_u32 s9, s3, 0
	s_mov_b32 s22, 1
	s_mov_b64 s[2:3], 0
	s_branch .LBB0_1330
